# speedup vs baseline: 1.0145x; 1.0145x over previous
.LBB5_223:
	s_or_b64 exec, exec, s[0:1]
	s_movk_i32 s6, 0x290
	v_mad_u32_u24 v26, v77, s6, v74
	s_waitcnt lgkmcnt(0)
	s_barrier
	ds_read_b128 v[28:31], v26
	s_mov_b32 s8, 0xf800000
	s_movk_i32 s7, 0x140
	s_waitcnt vmcnt(2) lgkmcnt(0)
	v_pk_add_f32 v[28:29], v[22:23], v[28:29]
	v_pk_add_f32 v[30:31], v[24:25], v[30:31]
	v_add_f32_e32 v22, v28, v29
	v_add_f32_e32 v22, v22, v30
	v_add_f32_e32 v22, v22, v31
	s_nop 1
	v_mov_b32_dpp v24, v22 quad_perm:[1,0,3,2] row_mask:0xf bank_mask:0xf
	s_waitcnt lgkmcnt(0)
	v_add_f32_e32 v22, v22, v24
	s_nop 1
	v_mov_b32_dpp v25, v22 quad_perm:[2,3,0,1] row_mask:0xf bank_mask:0xf
	s_waitcnt lgkmcnt(0)
	v_add_f32_e32 v22, v22, v25
	s_nop 1
	v_mov_b32_dpp v25, v22 row_half_mirror row_mask:0xf bank_mask:0xf
	s_waitcnt lgkmcnt(0)
	v_add_f32_e32 v22, v22, v25
	s_nop 1
	v_mov_b32_dpp v25, v22 row_mirror row_mask:0xf bank_mask:0xf
	s_waitcnt lgkmcnt(0)
	v_add_f32_e32 v22, v22, v25
	v_mov_b32_e32 v25, v22
	s_nop 1
	v_permlane16_swap_b32_e32 v22, v25
	s_waitcnt lgkmcnt(0)
	v_add_f32_e32 v22, v22, v25
	v_mul_f32_e32 v22, 0x3c000000, v22
	v_pk_add_f32 v[28:29], v[28:29], v[22:23] op_sel_hi:[1,0] neg_lo:[0,1] neg_hi:[0,1]
	v_pk_add_f32 v[30:31], v[30:31], v[22:23] op_sel_hi:[1,0] neg_lo:[0,1] neg_hi:[0,1]
	v_pk_mul_f32 v[32:33], v[28:29], v[28:29]
	v_pk_mul_f32 v[34:35], v[30:31], v[30:31]
	v_add_f32_e32 v22, v32, v33
	v_add_f32_e32 v22, v34, v22
	v_add_f32_e32 v22, v35, v22
	s_nop 1
	v_mov_b32_dpp v25, v22 quad_perm:[1,0,3,2] row_mask:0xf bank_mask:0xf
	v_mov_b64_e32 v[32:33], s[4:5]
	v_mad_i64_i32 v[32:33], s[0:1], v70, s7, v[32:33]
	s_waitcnt lgkmcnt(0)
	v_add_f32_e32 v22, v22, v25
	s_nop 1
	v_mov_b32_dpp v25, v22 quad_perm:[2,3,0,1] row_mask:0xf bank_mask:0xf
	s_waitcnt lgkmcnt(0)
	v_add_f32_e32 v22, v22, v25
	s_nop 1
	v_mov_b32_dpp v25, v22 row_half_mirror row_mask:0xf bank_mask:0xf
	s_waitcnt lgkmcnt(0)
	v_add_f32_e32 v25, v22, v25
	s_nop 1
	v_mov_b32_dpp v27, v25 row_mirror row_mask:0xf bank_mask:0xf
	v_mov_b32_e32 v99, 0x3727c5ac
	v_mov_b32_e32 v22, 0x260
	s_waitcnt lgkmcnt(0)
	v_add_f32_e32 v25, v25, v27
	v_mov_b32_e32 v27, v25
	s_nop 1
	v_permlane16_swap_b32_e32 v25, v27
	v_lshlrev_b32_e32 v0, 1, v1
	v_mov_b32_e32 v1, 0
	v_lshl_add_u64 v[32:33], v[32:33], 0, v[0:1]
	s_waitcnt lgkmcnt(0)
	v_add_f32_e32 v25, v25, v27
	v_fmamk_f32 v25, v25, 0x3c000000, v99
	v_mul_f32_e32 v27, 0x4f800000, v25
	v_cmp_gt_f32_e32 vcc, s8, v25
	s_nop 1
	v_cndmask_b32_e32 v25, v25, v27, vcc
	v_sqrt_f32_e32 v27, v25
	s_nop 0
	v_add_u32_e32 v34, -1, v27
	v_add_u32_e32 v35, 1, v27
	v_fma_f32 v36, -v34, v27, v25
	v_fma_f32 v37, -v35, v27, v25
	v_cmp_ge_f32_e64 s[0:1], 0, v36
	s_nop 1
	v_cndmask_b32_e64 v27, v27, v34, s[0:1]
	v_cmp_lt_f32_e64 s[0:1], 0, v37
	s_nop 1
	v_cndmask_b32_e64 v27, v27, v35, s[0:1]
	v_mul_f32_e32 v34, 0x37800000, v27
	v_cndmask_b32_e32 v27, v27, v34, vcc
	v_cmp_class_f32_e32 vcc, v25, v22
	s_nop 1
	v_cndmask_b32_e32 v25, v27, v25, vcc
	v_div_scale_f32 v27, s[0:1], v25, v25, 1.0
	v_rcp_f32_e32 v34, v27
	v_div_scale_f32 v0, vcc, 1.0, v25, 1.0
	v_fma_f32 v35, -v27, v34, 1.0
	v_fmac_f32_e32 v34, v35, v34
	v_mul_f32_e32 v35, v0, v34
	v_fma_f32 v36, -v27, v35, v0
	v_fmac_f32_e32 v35, v36, v34
	v_fma_f32 v0, -v27, v35, v0
	v_div_fmas_f32 v0, v0, v34, v35
	v_div_fixup_f32 v0, v0, v25, 1.0
	v_pk_mul_f32 v[28:29], v[28:29], v[0:1] op_sel_hi:[1,0]
	v_pk_mul_f32 v[30:31], v[30:31], v[0:1] op_sel_hi:[1,0]
	s_waitcnt vmcnt(0)
	v_pk_fma_f32 v[10:11], v[10:11], v[28:29], v[14:15]
	v_pk_fma_f32 v[12:13], v[12:13], v[30:31], v[16:17]
	v_cvt_pk_f16_f32 v10, v10, v11
	v_cvt_pk_f16_f32 v11, v12, v13
	s_andn2_b64 vcc, exec, s[2:3]
	global_store_dwordx2 v[32:33], v[10:11], off
	s_cbranch_vccnz .LBB5_225
	v_mad_u32_u24 v0, v75, s6, v72
	ds_read_b128 v[10:13], v0 offset:512
	s_waitcnt lgkmcnt(0)
	v_pk_add_f32 v[10:11], v[18:19], v[10:11]
	v_pk_add_f32 v[12:13], v[20:21], v[12:13]
	v_add_f32_e32 v0, v10, v11
	v_add_f32_e32 v0, v0, v12
	v_add_f32_e32 v0, v0, v13
	s_nop 1
	v_mov_b32_dpp v14, v0 quad_perm:[1,0,3,2] row_mask:0xf bank_mask:0xf
	s_waitcnt lgkmcnt(0)
	v_add_f32_e32 v0, v0, v14
	s_nop 1
	v_mov_b32_dpp v14, v0 quad_perm:[2,3,0,1] row_mask:0xf bank_mask:0xf
	s_waitcnt lgkmcnt(0)
	v_add_f32_e32 v0, v0, v14
	s_nop 1
	v_mov_b32_dpp v14, v0 row_half_mirror row_mask:0xf bank_mask:0xf
	s_waitcnt lgkmcnt(0)
	v_add_f32_e32 v0, v0, v14
	v_mul_f32_e32 v0, 0x3d000000, v0
	v_pk_add_f32 v[10:11], v[10:11], v[0:1] op_sel_hi:[1,0] neg_lo:[0,1] neg_hi:[0,1]
	v_pk_add_f32 v[12:13], v[12:13], v[0:1] op_sel_hi:[1,0] neg_lo:[0,1] neg_hi:[0,1]
	v_pk_mul_f32 v[14:15], v[10:11], v[10:11]
	v_pk_mul_f32 v[16:17], v[12:13], v[12:13]
	v_add_f32_e32 v0, v14, v15
	v_add_f32_e32 v0, v16, v0
	v_add_f32_e32 v0, v17, v0
	s_nop 1
	v_mov_b32_dpp v14, v0 quad_perm:[1,0,3,2] row_mask:0xf bank_mask:0xf
	s_waitcnt lgkmcnt(0)
	v_add_f32_e32 v0, v0, v14
	s_nop 1
	v_mov_b32_dpp v14, v0 quad_perm:[2,3,0,1] row_mask:0xf bank_mask:0xf
	s_waitcnt lgkmcnt(0)
	v_add_f32_e32 v0, v0, v14
	s_nop 1
	v_mov_b32_dpp v14, v0 row_half_mirror row_mask:0xf bank_mask:0xf
	s_waitcnt lgkmcnt(0)
	v_add_f32_e32 v0, v0, v14
	v_fmac_f32_e32 v99, 0x3d000000, v0
	v_mul_f32_e32 v0, 0x4f800000, v99
	v_cmp_gt_f32_e32 vcc, s8, v99
	v_mov_b64_e32 v[14:15], s[4:5]
	s_nop 0
	v_cndmask_b32_e32 v16, v99, v0, vcc
	v_sqrt_f32_e32 v17, v16
	v_lshlrev_b32_e32 v0, 1, v71
	v_add_u32_e32 v18, -1, v17
	v_add_u32_e32 v19, 1, v17
	v_fma_f32 v20, -v18, v17, v16
	v_fma_f32 v21, -v19, v17, v16
	v_cmp_ge_f32_e64 s[0:1], 0, v20
	s_nop 1
	v_cndmask_b32_e64 v17, v17, v18, s[0:1]
	v_cmp_lt_f32_e64 s[0:1], 0, v21
	s_nop 1
	v_cndmask_b32_e64 v17, v17, v19, s[0:1]
	v_mul_f32_e32 v18, 0x37800000, v17
	v_cndmask_b32_e32 v17, v17, v18, vcc
	v_cmp_class_f32_e32 vcc, v16, v22
	v_mad_i64_i32 v[14:15], s[0:1], v68, s7, v[14:15]
	s_nop 0
	v_cndmask_b32_e32 v16, v17, v16, vcc
	v_div_scale_f32 v17, s[0:1], v16, v16, 1.0
	v_rcp_f32_e32 v18, v17
	v_div_scale_f32 v19, vcc, 1.0, v16, 1.0
	v_lshl_add_u64 v[0:1], v[14:15], 0, v[0:1]
	v_fma_f32 v20, -v17, v18, 1.0
	v_fmac_f32_e32 v18, v20, v18
	v_mul_f32_e32 v20, v19, v18
	v_fma_f32 v21, -v17, v20, v19
	v_fmac_f32_e32 v20, v21, v18
	v_fma_f32 v17, -v17, v20, v19
	v_div_fmas_f32 v17, v17, v18, v20
	v_div_fixup_f32 v16, v17, v16, 1.0
	v_pk_mul_f32 v[10:11], v[10:11], v[16:17] op_sel_hi:[1,0]
	v_pk_mul_f32 v[12:13], v[12:13], v[16:17] op_sel_hi:[1,0]
	v_pk_fma_f32 v[2:3], v[2:3], v[10:11], v[6:7]
	v_pk_fma_f32 v[4:5], v[4:5], v[12:13], v[8:9]
	v_cvt_pk_f16_f32 v2, v2, v3
	v_cvt_pk_f16_f32 v3, v4, v5
	global_store_dwordx2 v[0:1], v[2:3], off offset:256
